# lru_a balanced 132-tile split per workgroup plus removal of 32 dead fp8 destination initialisations in the DN epilogue
# speedup vs baseline: 1.0161x; 1.0116x over previous
; #define LAS __attribute__((address_space(3)))
; __device__ __forceinline__ void ph_lru_a(const Frame& F, int jj) {
;     ...
;     for (int task = F.wg; task < NTASK; task += F.G) {
;         const int grp = task % 11, kb = (task / 11) & 15, b = task / (11 * 16);
;         __syncthreads();
;         for (int i = F.tid; i < 4 * 4096 / 8; i += 512) { const int mg = i >> 9, r = i & 511;
;             *(LAS u32x4*)(Wl + (mg * 64 + (r >> 3)) * 72 + (r & 7) * 8) = *(const u32x4*)(wsrc + ((size_t)mg * 16 + kb) * 4096 + r * 8); }
;         for (int i = F.tid; i < 11 * 64; i += 512) { const int kind = i >> 6, ch = kb * 64 + (i & 63); float v;
;             if (kind < 4) v = cw[kind * 1024 + ch]; else if (kind == 4) v = cb[ch];
;             else { const int d = (kind - 5) / 3, w = (kind - 5) % 3; v = (w == 0) ? b_a[d * 1024 + ch] : (w == 1) ? b_x[d * 1024 + ch] : -8.0f * log1pf(__expf(-lam[d * 1024 + ch])); }
;             CT[i] = v; }
;         __syncthreads();
;         const int nt0 = grp * 48;
;         LruRaw raw; lru_load(F, b, kb, nt0 + F.wave, raw);
.LBB0_434:
	v_cndmask_b32_e64 v0, 0, 1, s[86:87]
	s_andn2_b64 vcc, exec, s[0:1]
	v_cmp_ne_u32_e64 s[40:41], 1, v0
	s_cbranch_vccnz .LBB0_749
	s_and_b64 vcc, exec, s[40:41]
	s_mov_b64 s[0:1], -1
	s_cbranch_vccnz .LBB0_473
	v_readlane_b32 s0, v254, 30
	s_waitcnt vmcnt(0)
	v_mov_b32_e32 v4, v177
	v_readlane_b32 s5, v254, 31
	v_mov_b32_e32 v0, s0
	ds_read_b128 v[6:9], v0
	v_mov_b32_e32 v0, s5
	ds_read_b64 v[0:1], v0
	v_readlane_b32 s7, v254, 32
	v_readlane_b32 s14, v251, 6
	s_waitcnt lgkmcnt(0)
	v_readfirstlane_b32 s1, v7
	v_readfirstlane_b32 s4, v6
	v_readfirstlane_b32 s6, v0
	v_mov_b32_e32 v0, s7
	v_readfirstlane_b32 s0, v9
	v_readfirstlane_b32 s2, v8
	ds_read2_b64 v[6:9], v0 offset1:1
	v_readlane_b32 s15, v251, 7
	s_mov_b32 s22, s26
	v_readfirstlane_b32 s5, v1
	s_and_b64 vcc, exec, s[14:15]
	s_waitcnt lgkmcnt(0)
	v_readfirstlane_b32 s8, v7
	v_readfirstlane_b32 s10, v6
	v_readfirstlane_b32 s7, v9
	v_readfirstlane_b32 s9, v8
	s_cbranch_vccz .LBB0_472
	s_mov_b32 s14, s22
	s_mov_b32 s15, s65
	s_lshl_b64 s[16:17], s[14:15], 14
	s_lshl_b64 s[20:21], s[14:15], 12
	s_add_u32 s52, s4, s16
	s_addc_u32 s53, s1, s17
	s_add_u32 s58, s2, s20
	s_addc_u32 s59, s0, s21
	s_lshl_b64 s[16:17], s[14:15], 13
	s_add_u32 s66, s6, s16
	s_addc_u32 s67, s5, s17
	s_add_u32 s0, s10, s16
	v_add_u32_e32 v3, s79, v4
	s_addc_u32 s1, s8, s17
	s_movk_i32 s2, 0x800
	s_add_u32 s4, s9, s16
	v_cmp_gt_i32_e64 s[42:43], s2, v3
	s_movk_i32 s2, 0x2c0
	v_and_b32_e32 v5, 0x1ff, v3
	v_and_b32_e32 v94, -16, v4
	s_addc_u32 s5, s7, s17
	v_cmp_gt_i32_e64 s[44:45], s2, v3
	v_lshlrev_b32_e32 v6, 4, v5
	v_readlane_b32 s6, v255, 4
	v_lshlrev_b32_e32 v5, 2, v94
	v_readlane_b32 s2, v254, 33
	v_mov_b32_e32 v7, v2
	v_readlane_b32 s7, v255, 5
	v_add_u32_e32 v107, s2, v5
	s_add_i32 s2, 0, 0x11800
	v_lshl_add_u64 v[6:7], s[6:7], 0, v[6:7]
	s_mov_b64 s[6:7], 0x6ba0000
	v_add_u32_e32 v108, s2, v5
	v_readlane_b32 s2, v252, 20
	v_and_b32_e32 v104, 15, v4
	v_lshl_add_u64 v[92:93], v[6:7], 0, s[6:7]
	v_mov_b32_e32 v6, s2
	s_movk_i32 s2, 0x110
	v_mad_u32_u24 v6, v104, s2, v6
	v_readlane_b32 s2, v254, 34
	v_add_u32_e32 v109, v6, v5
	v_lshlrev_b32_e32 v5, 1, v4
	v_add_u32_e32 v111, s2, v94
	v_readlane_b32 s2, v254, 35
	v_ashrrev_i32_e32 v0, 2, v4
	v_and_b32_e32 v5, 0xffffffe0, v5
	v_add_u32_e32 v112, s2, v94
	v_readlane_b32 s2, v254, 36
	v_and_b32_e32 v0, -4, v0
	v_ashrrev_i32_e32 v95, 31, v94
	v_add_u32_e32 v113, s2, v94
	s_add_i32 s2, 0, 0x12000
	v_add_u32_e32 v115, s2, v94
	v_readlane_b32 s2, v254, 37
	v_add_u32_e32 v110, v6, v5
	v_sub_u32_e32 v5, 0, v94
	v_add_u32_e32 v116, s2, v94
	v_readlane_b32 s2, v254, 38
	v_mul_u32_u24_e32 v6, 0x90, v104
	v_ashrrev_i32_e32 v1, 31, v0
	v_add_u32_e32 v117, s2, v94
	v_readlane_b32 s2, v253, 56
	v_bfe_u32 v105, v3, 3, 6
	v_and_b32_e32 v106, 63, v4
	v_lshl_add_u32 v118, v4, 3, s2
	v_readlane_b32 s2, v253, 31
	v_add3_u32 v114, 0, v6, v94
	v_lshl_add_u64 v[96:97], v[94:95], 1, s[82:83]
	v_lshl_add_u32 v119, v4, 2, s2
	v_add_u32_e32 v120, v110, v5
	s_movk_i32 s101, 0x2bf
	s_cmpk_eq_i32 s3, 0x100
	s_cselect_b32 s100, 0x7b, 39
	s_cselect_b32 s101, 0xff, s101
	s_mov_b32 s11, s89
	s_branch .LBB0_439

; #define LAS __attribute__((address_space(3)))
; __device__ __forceinline__ void ph_lru_a(const Frame& F, int jj) {
;     ...
;     for (int task = F.wg; task < NTASK; task += F.G) {
;         const int grp = task % 11, kb = (task / 11) & 15, b = task / (11 * 16);
;         __syncthreads();
;         for (int i = F.tid; i < 4 * 4096 / 8; i += 512) { const int mg = i >> 9, r = i & 511;
;             *(LAS u32x4*)(Wl + (mg * 64 + (r >> 3)) * 72 + (r & 7) * 8) = *(const u32x4*)(wsrc + ((size_t)mg * 16 + kb) * 4096 + r * 8); }
.LBB0_439:
	s_mul_hi_i32 s13, s11, 0x2e8ba2e9
	s_lshr_b32 s16, s13, 31
	s_ashr_i32 s10, s13, 1
	s_add_i32 s10, s10, s16
	s_lshr_b32 s14, s11, 2
	s_cmpk_eq_i32 s101, 0xff
	s_cselect_b32 s10, s14, s10
	s_and_b32 s2, s10, 15
	s_waitcnt vmcnt(0)
	s_barrier
	s_and_saveexec_b64 s[6:7], s[42:43]
	s_movk_i32 s14, 0x90
	s_cbranch_execz .LBB0_442
	s_lshl_b32 s64, s2, 13
	v_lshl_add_u64 v[4:5], v[92:93], 0, s[64:65]
	s_mov_b64 s[8:9], 0x20000
	global_load_dwordx4 v[210:213], v[4:5], off
	v_lshl_add_u64 v[226:227], v[4:5], 0, s[8:9]
	global_load_dwordx4 v[214:217], v[226:227], off
	v_lshl_add_u64 v[226:227], v[226:227], 0, s[8:9]
	global_load_dwordx4 v[218:221], v[226:227], off
	v_lshl_add_u64 v[226:227], v[226:227], 0, s[8:9]
	global_load_dwordx4 v[222:225], v[226:227], off
	v_and_b32_e32 v13, 56, v118
	s_movk_i32 s17, 0x5ff
	v_lshlrev_b32_e32 v13, 1, v13
	v_mul_lo_u32 v12, v105, s14
	v_add3_u32 v12, 0, v12, v13
	s_waitcnt vmcnt(0)
	ds_write_b128 v12, v[210:213]
	ds_write_b128 v12, v[214:217] offset:9216
	ds_write_b128 v12, v[218:221] offset:18432
	ds_write_b128 v12, v[222:225] offset:27648

; __device__ __forceinline__ void lru_load(const Frame& F, int b, int kb, int nt, LruRaw& R) {
;     const bf16_t* P = (const bf16_t*)(F.R1 + R1_P);
;     const int tk = F.lane & 15, g = F.lane >> 4;
;     const int len = nt < 16 ? CTXL : SEQ, tpos = (nt < 16 ? nt * 16 : (nt - 16) * 16) + tk;
;     const bf16_t* pbase = P + (size_t)((nt < 16 ? b * CTXL : TC + b * SEQ)) * 2048 + 1024 + kb * 64 + g * 16;
;     unsigned okm = 0u;
; #pragma unroll
;     for (int tap = 0; tap < 4; ++tap) { const int tp = tpos + tap - 2; const bool ok = (tp >= 0 && tp < len); const bf16_t* pr = pbase + (size_t)(ok ? tp : tpos) * 2048;
;         okm |= ok ? (1u << tap) : 0u;
;         R.a[tap] = *(const u32x4*)pr; R.b[tap] = *(const u32x4*)(pr + 8); }
;     R.ok = okm;
; __device__ __forceinline__ void ph_lru_a(const Frame& F, int jj) {
;     ...
;         const int nt0 = grp * 48;
;         LruRaw raw; lru_load(F, b, kb, nt0 + F.wave, raw);
;         for (int ti = F.wave; ti < 48; ti += 8) {
;             const int nt = nt0 + ti;
;             float av[2][4][4], xv[2][4][4]; unsigned pw[2][4][4];
;             lru_conv(F, raw, CT, ucb);
;             lru_load(F, b, kb, nt0 + min(ti + 8, 40 + F.wave), raw);
;             lru_gates(F, Wl, CT, ucb, av, pw);
;             const int row = lru_row(b, nt, tk);
.LBB0_463:
	s_or_b64 exec, exec, s[6:7]
	v_readlane_b32 s6, v251, 8
	v_readlane_b32 s7, v251, 9
	s_andn2_b64 vcc, exec, s[6:7]
	s_waitcnt lgkmcnt(0)
	s_barrier
	s_cbranch_vccnz .LBB0_438
	s_mul_i32 s2, s10, 11
	s_sub_i32 s2, s11, s2
	s_mul_i32 s2, s2, 48
	s_and_b32 s6, s11, 3
	s_mulk_i32 s6, 0x84
	s_cmpk_eq_i32 s101, 0xff
	s_cselect_b32 s2, s6, s2
	s_add_i32 s6, s2, s75
	s_lshl_b32 s7, s6, 4
	s_cmp_lt_i32 s6, 16
	s_cselect_b32 s17, 0x100, s88
	s_add_i32 s8, s7, 0xffffff00
	s_cmp_lt_i32 s6, 16
	s_cselect_b32 s20, s7, s8
	s_ashr_i32 s7, s13, 5
	s_add_i32 s21, s7, s16
	s_lshr_b32 s7, s11, 6
	s_cmpk_eq_i32 s101, 0xff
	s_cselect_b32 s21, s7, s21
	s_lshl_b32 s24, s21, 13
	s_lshl_b32 s13, s21, 8
	s_or_b32 s16, s24, 0x400
	s_cmp_lt_i32 s6, 16
	s_cselect_b32 s6, s13, s16
	s_ashr_i32 s7, s6, 31
	s_lshl_b64 s[6:7], s[6:7], 12
	s_add_u32 s6, s82, s6
	v_or_b32_e32 v14, s20, v104
	s_addc_u32 s7, s83, s7
	s_lshl_b32 s8, s64, 1
	v_add_u32_e32 v4, 1, v14
	s_add_u32 s6, s6, s8
	v_cmp_lt_i32_e32 vcc, -2, v14
	v_cmp_gt_i32_e64 s[46:47], s17, v4
	s_addc_u32 s7, s7, 0
	s_and_b64 vcc, vcc, s[46:47]
	s_cmp_gt_i32 s20, -1
	v_lshl_add_u64 v[12:13], v[94:95], 1, s[6:7]
	s_cselect_b64 s[6:7], -1, 0
	v_cmp_gt_i32_e64 s[46:47], s17, v14
	s_and_b64 s[6:7], s[6:7], s[46:47]
	v_cmp_lt_i32_e64 s[46:47], 0, v14
	v_cmp_ge_i32_e64 s[48:49], s17, v14
	v_add_u32_e32 v26, -2, v14
	s_and_b64 s[46:47], s[46:47], s[48:49]
	v_cmp_lt_i32_e64 s[48:49], 1, v14
	v_cmp_gt_i32_e64 s[50:51], s17, v26
	v_cndmask_b32_e64 v15, 0, 4, s[6:7]
	v_cndmask_b32_e64 v16, 0, 2, s[46:47]
	s_and_b64 s[48:49], s[48:49], s[50:51]
	v_cndmask_b32_e32 v4, v14, v4, vcc
	v_or_b32_e32 v15, v15, v16
	v_cndmask_b32_e64 v16, 0, 1, s[48:49]
	v_cndmask_b32_e64 v17, 0, 8, vcc
	v_ashrrev_i32_e32 v5, 31, v4
	v_or3_b32 v36, v15, v16, v17
	v_ashrrev_i32_e32 v15, 31, v14
	v_lshlrev_b64 v[4:5], 12, v[4:5]
	v_lshlrev_b64 v[16:17], 12, v[14:15]
	v_lshl_add_u64 v[8:9], v[12:13], 0, v[4:5]
	v_lshl_add_u64 v[20:21], v[12:13], 0, v[16:17]
	global_load_dwordx4 v[4:7], v[8:9], off offset:2064
	s_nop 0
	global_load_dwordx4 v[8:11], v[8:9], off offset:2048
	s_nop 0
	global_load_dwordx4 v[16:19], v[20:21], off offset:2064
	global_load_dwordx4 v[28:31], v[20:21], off offset:2048
	v_subbrev_co_u32_e64 v20, vcc, 0, v14, s[46:47]
	v_ashrrev_i32_e32 v21, 31, v20
	v_cndmask_b32_e64 v14, v14, v26, s[48:49]
	v_lshlrev_b64 v[20:21], 12, v[20:21]
	v_ashrrev_i32_e32 v15, 31, v14
	v_lshl_add_u64 v[24:25], v[12:13], 0, v[20:21]
	v_lshlrev_b64 v[14:15], 12, v[14:15]
	global_load_dwordx4 v[20:23], v[24:25], off offset:2064
	global_load_dwordx4 v[32:35], v[24:25], off offset:2048
	v_lshl_add_u64 v[24:25], v[12:13], 0, v[14:15]
	global_load_dwordx4 v[12:15], v[24:25], off offset:2064
	s_nop 0
	global_load_dwordx4 v[24:27], v[24:25], off offset:2048
	s_mov_b32 s9, s65
	s_or_b32 s17, s24, 0x300
	s_lshl_b32 s6, s64, 2
	v_readlane_b32 s7, v251, 2
	s_add_u32 s6, s7, s6
	v_readlane_b32 s7, v251, 3
	v_lshl_add_u64 v[100:101], v[96:97], 0, s[8:9]
	s_mov_b32 s8, s2
	s_addc_u32 s7, s7, 0
	v_readlane_b32 s14, v251, 4
	s_add_i32 s8, s75, s8
	v_lshl_add_u64 v[38:39], s[64:65], 0, v[0:1]
	s_lshl_b32 s26, s21, 1
	v_readlane_b32 s15, v251, 5
	s_or_b32 s27, s26, 1
	v_lshl_add_u64 v[98:99], v[38:39], 2, s[14:15]
	v_lshl_or_b32 v121, s8, 4, v104
	s_mov_b32 s30, s75
	s_waitcnt vmcnt(0)
	s_branch .LBB0_466

;     __device__ __forceinline__ void operator()(const f32x4 (&acc)[2][2][4][2], const Unit& u, int wr, int wc, int fr, int fq) const {
;         const int row0 = u.pm * BM + wr * 64 + fr, col0 = u.pn * BM + wc * 64 + 16 * fq;
;         unsigned char* yb = Y + (size_t)row0 * DM + col0;
; #pragma unroll
;         for (int ai = 0; ai < 2; ++ai)
; #pragma unroll
;             for (int m = 0; m < 4; ++m) { const int rl = ai * HALF + m * 16;
;                 u32x4 ww; unsigned pk[4];
; #pragma unroll
;                 for (int bj = 0; bj < 2; ++bj)
; #pragma unroll
;                     for (int n = 0; n < 2; ++n) { f32x4 v = acc[ai][bj][m][n] * 16.0f;
; #pragma unroll
;                         for (int j = 0; j < 4; ++j) v[j] = __builtin_amdgcn_fmed3f(v[j], -440.0f, 440.0f);
;                         int p = __builtin_amdgcn_cvt_pk_fp8_f32(v[0], v[1], 0, false); p = __builtin_amdgcn_cvt_pk_fp8_f32(v[2], v[3], p, true); pk[bj * 2 + n] = (unsigned)p; }
;                 ww.x = pk[0]; ww.y = pk[1]; ww.z = pk[2]; ww.w = pk[3];
;                 *(u32x4*)(yb + (size_t)rl * DM) = ww;
;                 asm volatile("" ::: "memory"); }
.LBB0_1634:
	v_pk_mul_f32 v[128:129], v[128:129], s[74:75] op_sel_hi:[1,0]
	v_pk_mul_f32 v[130:131], v[130:131], s[74:75] op_sel_hi:[1,0]
	v_med3_f32 v3, v128, s95, v189
	v_med3_f32 v129, v129, s95, v189
	v_cvt_pk_fp8_f32 v128, v3, v129
	v_pk_mul_f32 v[124:125], v[124:125], s[74:75] op_sel_hi:[1,0]
	v_med3_f32 v130, v130, s95, v189
	v_med3_f32 v131, v131, s95, v189
	v_med3_f32 v3, v124, s95, v189
	v_med3_f32 v124, v125, s95, v189
	v_pk_mul_f32 v[120:121], v[120:121], s[74:75] op_sel_hi:[1,0]
	v_cvt_pk_fp8_f32 v128, v130, v131 op_sel:[0,0,1]
	v_cvt_pk_fp8_f32 v129, v3, v124
	v_med3_f32 v3, v120, s95, v189
	v_med3_f32 v120, v121, s95, v189
	v_pk_mul_f32 v[116:117], v[116:117], s[74:75] op_sel_hi:[1,0]
	v_cvt_pk_fp8_f32 v130, v3, v120
	v_med3_f32 v3, v116, s95, v189
	v_med3_f32 v116, v117, s95, v189
	v_pk_mul_f32 v[112:113], v[112:113], s[74:75] op_sel_hi:[1,0]
	v_cvt_pk_fp8_f32 v131, v3, v116
	v_med3_f32 v3, v112, s95, v189
	v_med3_f32 v113, v113, s95, v189
	v_cvt_pk_fp8_f32 v112, v3, v113
	v_pk_mul_f32 v[114:115], v[114:115], s[74:75] op_sel_hi:[1,0]
	v_pk_mul_f32 v[108:109], v[108:109], s[74:75] op_sel_hi:[1,0]
	v_med3_f32 v114, v114, s95, v189
	v_med3_f32 v115, v115, s95, v189
	v_med3_f32 v3, v108, s95, v189
	v_med3_f32 v108, v109, s95, v189
	v_pk_mul_f32 v[104:105], v[104:105], s[74:75] op_sel_hi:[1,0]
	v_cvt_pk_fp8_f32 v112, v114, v115 op_sel:[0,0,1]
	v_cvt_pk_fp8_f32 v113, v3, v108
	v_med3_f32 v3, v104, s95, v189
	v_med3_f32 v104, v105, s95, v189
	v_pk_mul_f32 v[100:101], v[100:101], s[74:75] op_sel_hi:[1,0]
	v_cvt_pk_fp8_f32 v114, v3, v104
	v_med3_f32 v3, v100, s95, v189
	v_med3_f32 v100, v101, s95, v189
	v_pk_mul_f32 v[96:97], v[96:97], s[74:75] op_sel_hi:[1,0]
	v_cvt_pk_fp8_f32 v115, v3, v100
	v_med3_f32 v3, v96, s95, v189
	v_med3_f32 v97, v97, s95, v189
	v_cvt_pk_fp8_f32 v96, v3, v97
	v_pk_mul_f32 v[98:99], v[98:99], s[74:75] op_sel_hi:[1,0]
	v_pk_mul_f32 v[92:93], v[92:93], s[74:75] op_sel_hi:[1,0]
	v_med3_f32 v98, v98, s95, v189
	v_med3_f32 v99, v99, s95, v189
	v_med3_f32 v3, v92, s95, v189
	v_med3_f32 v92, v93, s95, v189
	v_pk_mul_f32 v[88:89], v[88:89], s[74:75] op_sel_hi:[1,0]
	v_cvt_pk_fp8_f32 v96, v98, v99 op_sel:[0,0,1]
	v_cvt_pk_fp8_f32 v97, v3, v92
	v_med3_f32 v3, v88, s95, v189
	v_med3_f32 v88, v89, s95, v189
	v_pk_mul_f32 v[84:85], v[84:85], s[74:75] op_sel_hi:[1,0]
	v_cvt_pk_fp8_f32 v98, v3, v88
	v_med3_f32 v3, v84, s95, v189
	v_med3_f32 v84, v85, s95, v189
	v_pk_mul_f32 v[80:81], v[80:81], s[74:75] op_sel_hi:[1,0]
	v_cvt_pk_fp8_f32 v99, v3, v84
	v_med3_f32 v3, v80, s95, v189
	v_med3_f32 v81, v81, s95, v189
	v_cvt_pk_fp8_f32 v80, v3, v81
	v_pk_mul_f32 v[82:83], v[82:83], s[74:75] op_sel_hi:[1,0]
	v_pk_mul_f32 v[76:77], v[76:77], s[74:75] op_sel_hi:[1,0]
	v_med3_f32 v82, v82, s95, v189
	v_med3_f32 v83, v83, s95, v189
	v_med3_f32 v3, v76, s95, v189
	v_med3_f32 v76, v77, s95, v189
	v_pk_mul_f32 v[72:73], v[72:73], s[74:75] op_sel_hi:[1,0]
	v_cvt_pk_fp8_f32 v80, v82, v83 op_sel:[0,0,1]
	v_cvt_pk_fp8_f32 v81, v3, v76
	v_med3_f32 v3, v72, s95, v189
	v_med3_f32 v72, v73, s95, v189
	v_pk_mul_f32 v[68:69], v[68:69], s[74:75] op_sel_hi:[1,0]
	v_cvt_pk_fp8_f32 v82, v3, v72
	v_med3_f32 v3, v68, s95, v189
	v_med3_f32 v68, v69, s95, v189
	v_pk_mul_f32 v[64:65], v[64:65], s[74:75] op_sel_hi:[1,0]
	v_cvt_pk_fp8_f32 v83, v3, v68
	v_med3_f32 v3, v64, s95, v189
	v_med3_f32 v65, v65, s95, v189
	v_cvt_pk_fp8_f32 v64, v3, v65
	v_pk_mul_f32 v[66:67], v[66:67], s[74:75] op_sel_hi:[1,0]
	v_pk_mul_f32 v[60:61], v[60:61], s[74:75] op_sel_hi:[1,0]
	v_med3_f32 v66, v66, s95, v189
	v_med3_f32 v67, v67, s95, v189
	v_med3_f32 v3, v60, s95, v189
	v_med3_f32 v60, v61, s95, v189
	v_pk_mul_f32 v[56:57], v[56:57], s[74:75] op_sel_hi:[1,0]
	v_cvt_pk_fp8_f32 v64, v66, v67 op_sel:[0,0,1]
	v_cvt_pk_fp8_f32 v65, v3, v60
	v_med3_f32 v3, v56, s95, v189
	v_med3_f32 v56, v57, s95, v189
	v_pk_mul_f32 v[52:53], v[52:53], s[74:75] op_sel_hi:[1,0]
	v_cvt_pk_fp8_f32 v66, v3, v56
	v_med3_f32 v3, v52, s95, v189
	v_med3_f32 v52, v53, s95, v189
	v_pk_mul_f32 v[48:49], v[48:49], s[74:75] op_sel_hi:[1,0]
	v_cvt_pk_fp8_f32 v67, v3, v52
	v_med3_f32 v3, v48, s95, v189
	v_med3_f32 v49, v49, s95, v189
	v_cvt_pk_fp8_f32 v48, v3, v49
	v_pk_mul_f32 v[50:51], v[50:51], s[74:75] op_sel_hi:[1,0]
	v_pk_mul_f32 v[44:45], v[44:45], s[74:75] op_sel_hi:[1,0]
	v_med3_f32 v50, v50, s95, v189
	v_med3_f32 v51, v51, s95, v189
	v_med3_f32 v3, v44, s95, v189
	v_med3_f32 v44, v45, s95, v189
	v_pk_mul_f32 v[40:41], v[40:41], s[74:75] op_sel_hi:[1,0]
	v_cvt_pk_fp8_f32 v48, v50, v51 op_sel:[0,0,1]
	v_cvt_pk_fp8_f32 v49, v3, v44
	v_med3_f32 v3, v40, s95, v189
	v_med3_f32 v40, v41, s95, v189
	v_pk_mul_f32 v[36:37], v[36:37], s[74:75] op_sel_hi:[1,0]
	v_cvt_pk_fp8_f32 v50, v3, v40
	v_med3_f32 v3, v36, s95, v189
	v_med3_f32 v36, v37, s95, v189
	v_pk_mul_f32 v[32:33], v[32:33], s[74:75] op_sel_hi:[1,0]
	v_cvt_pk_fp8_f32 v51, v3, v36
	v_med3_f32 v3, v32, s95, v189
	v_med3_f32 v33, v33, s95, v189
	v_cvt_pk_fp8_f32 v32, v3, v33
	v_lshl_add_u32 v0, s20, 8, v136
	v_pk_mul_f32 v[34:35], v[34:35], s[74:75] op_sel_hi:[1,0]
	v_pk_mul_f32 v[28:29], v[28:29], s[74:75] op_sel_hi:[1,0]
	v_ashrrev_i32_e32 v1, 31, v0
	v_readlane_b32 s14, v252, 35
	v_med3_f32 v34, v34, s95, v189
	v_med3_f32 v35, v35, s95, v189
	v_med3_f32 v3, v28, s95, v189
	v_med3_f32 v28, v29, s95, v189
	v_pk_mul_f32 v[24:25], v[24:25], s[74:75] op_sel_hi:[1,0]
	v_lshl_or_b32 v140, s10, 8, v138
	v_lshlrev_b64 v[0:1], 10, v[0:1]
	v_readlane_b32 s15, v252, 36
	v_cvt_pk_fp8_f32 v32, v34, v35 op_sel:[0,0,1]
	v_cvt_pk_fp8_f32 v33, v3, v28
	v_med3_f32 v3, v24, s95, v189
	v_med3_f32 v24, v25, s95, v189
	v_pk_mul_f32 v[20:21], v[20:21], s[74:75] op_sel_hi:[1,0]
;     __device__ __forceinline__ void operator()(const f32x4 (&acc)[2][2][4][2], const Unit& u, int wr, int wc, int fr, int fq) const {
;         const int row0 = u.pm * BM + wr * 64 + fr, col0 = u.pn * BM + wc * 64 + 16 * fq;
;         unsigned char* yb = Y + (size_t)row0 * DM + col0;
; #pragma unroll
;         for (int ai = 0; ai < 2; ++ai)
; #pragma unroll
;             for (int m = 0; m < 4; ++m) { const int rl = ai * HALF + m * 16;
;                 u32x4 ww; unsigned pk[4];
; #pragma unroll
;                 for (int bj = 0; bj < 2; ++bj)
; #pragma unroll
;                     for (int n = 0; n < 2; ++n) { f32x4 v = acc[ai][bj][m][n] * 16.0f;
; #pragma unroll
;                         for (int j = 0; j < 4; ++j) v[j] = __builtin_amdgcn_fmed3f(v[j], -440.0f, 440.0f);
;                         int p = __builtin_amdgcn_cvt_pk_fp8_f32(v[0], v[1], 0, false); p = __builtin_amdgcn_cvt_pk_fp8_f32(v[2], v[3], p, true); pk[bj * 2 + n] = (unsigned)p; }
;                 ww.x = pk[0]; ww.y = pk[1]; ww.z = pk[2]; ww.w = pk[3];
;                 *(u32x4*)(yb + (size_t)rl * DM) = ww;
;                 asm volatile("" ::: "memory"); }
	v_lshl_add_u64 v[0:1], s[14:15], 0, v[0:1]
	v_ashrrev_i32_e32 v141, 31, v140
	v_cvt_pk_fp8_f32 v34, v3, v24
	v_med3_f32 v3, v20, s95, v189
	v_med3_f32 v20, v21, s95, v189
	v_pk_mul_f32 v[16:17], v[16:17], s[74:75] op_sel_hi:[1,0]
	v_lshl_add_u64 v[0:1], v[0:1], 0, v[140:141]
	v_pk_mul_f32 v[102:103], v[102:103], s[74:75] op_sel_hi:[1,0]
	s_movk_i32 s9, 0x4000
	v_cvt_pk_fp8_f32 v35, v3, v20
	v_med3_f32 v3, v16, s95, v189
	v_med3_f32 v17, v17, s95, v189
	v_med3_f32 v101, v102, s95, v189
	v_med3_f32 v102, v103, s95, v189
	v_add_co_u32_e32 v100, vcc, s9, v0
	v_cvt_pk_fp8_f32 v16, v3, v17
	v_pk_mul_f32 v[126:127], v[126:127], s[74:75] op_sel_hi:[1,0]
	v_pk_mul_f32 v[122:123], v[122:123], s[74:75] op_sel_hi:[1,0]
	v_pk_mul_f32 v[118:119], v[118:119], s[74:75] op_sel_hi:[1,0]
	v_cvt_pk_fp8_f32 v115, v101, v102 op_sel:[0,0,1]
	v_addc_co_u32_e32 v101, vcc, 0, v1, vcc
	v_pk_mul_f32 v[86:87], v[86:87], s[74:75] op_sel_hi:[1,0]
	v_med3_f32 v125, v126, s95, v189
	v_med3_f32 v126, v127, s95, v189
	v_med3_f32 v121, v122, s95, v189
	v_med3_f32 v122, v123, s95, v189
	v_med3_f32 v117, v118, s95, v189
	v_med3_f32 v118, v119, s95, v189
	v_pk_mul_f32 v[110:111], v[110:111], s[74:75] op_sel_hi:[1,0]
	v_pk_mul_f32 v[106:107], v[106:107], s[74:75] op_sel_hi:[1,0]
	v_med3_f32 v85, v86, s95, v189
	v_med3_f32 v86, v87, s95, v189
	v_add_co_u32_e32 v84, vcc, s39, v0
	v_pk_mul_f32 v[18:19], v[18:19], s[74:75] op_sel_hi:[1,0]
	v_pk_mul_f32 v[12:13], v[12:13], s[74:75] op_sel_hi:[1,0]
	v_cvt_pk_fp8_f32 v129, v125, v126 op_sel:[0,0,1]
	v_cvt_pk_fp8_f32 v130, v121, v122 op_sel:[0,0,1]
	v_cvt_pk_fp8_f32 v131, v117, v118 op_sel:[0,0,1]
	v_med3_f32 v109, v110, s95, v189
	v_med3_f32 v110, v111, s95, v189
	v_med3_f32 v105, v106, s95, v189
	v_med3_f32 v106, v107, s95, v189
	v_pk_mul_f32 v[94:95], v[94:95], s[74:75] op_sel_hi:[1,0]
	v_pk_mul_f32 v[90:91], v[90:91], s[74:75] op_sel_hi:[1,0]
	v_cvt_pk_fp8_f32 v99, v85, v86 op_sel:[0,0,1]
	v_addc_co_u32_e32 v85, vcc, 0, v1, vcc
	v_pk_mul_f32 v[70:71], v[70:71], s[74:75] op_sel_hi:[1,0]
	s_mov_b32 s9, 0xc000
	v_med3_f32 v18, v18, s95, v189
	v_med3_f32 v19, v19, s95, v189
	v_med3_f32 v3, v12, s95, v189
	v_med3_f32 v12, v13, s95, v189
	v_pk_mul_f32 v[8:9], v[8:9], s[74:75] op_sel_hi:[1,0]
	v_cvt_pk_fp8_f32 v113, v109, v110 op_sel:[0,0,1]
	v_cvt_pk_fp8_f32 v114, v105, v106 op_sel:[0,0,1]
	v_med3_f32 v93, v94, s95, v189
	v_med3_f32 v94, v95, s95, v189
	v_med3_f32 v89, v90, s95, v189
	v_med3_f32 v90, v91, s95, v189
	v_pk_mul_f32 v[78:79], v[78:79], s[74:75] op_sel_hi:[1,0]
	v_pk_mul_f32 v[74:75], v[74:75], s[74:75] op_sel_hi:[1,0]
	v_med3_f32 v69, v70, s95, v189
	v_med3_f32 v70, v71, s95, v189
	v_add_co_u32_e32 v68, vcc, s9, v0
	v_cvt_pk_fp8_f32 v16, v18, v19 op_sel:[0,0,1]
	v_cvt_pk_fp8_f32 v17, v3, v12
	v_med3_f32 v3, v8, s95, v189
	v_med3_f32 v8, v9, s95, v189
	v_pk_mul_f32 v[4:5], v[4:5], s[74:75] op_sel_hi:[1,0]
	v_cvt_pk_fp8_f32 v97, v93, v94 op_sel:[0,0,1]
	v_cvt_pk_fp8_f32 v98, v89, v90 op_sel:[0,0,1]
	v_med3_f32 v77, v78, s95, v189
	v_med3_f32 v78, v79, s95, v189
	v_med3_f32 v73, v74, s95, v189
	v_med3_f32 v74, v75, s95, v189
	v_cvt_pk_fp8_f32 v83, v69, v70 op_sel:[0,0,1]
	v_addc_co_u32_e32 v69, vcc, 0, v1, vcc
	v_pk_mul_f32 v[62:63], v[62:63], s[74:75] op_sel_hi:[1,0]
	v_pk_mul_f32 v[58:59], v[58:59], s[74:75] op_sel_hi:[1,0]
	v_pk_mul_f32 v[54:55], v[54:55], s[74:75] op_sel_hi:[1,0]
	s_mov_b32 s9, 0x20000
	v_cvt_pk_fp8_f32 v18, v3, v8
	v_med3_f32 v3, v4, s95, v189
	v_med3_f32 v4, v5, s95, v189
	v_cvt_pk_fp8_f32 v81, v77, v78 op_sel:[0,0,1]
	v_cvt_pk_fp8_f32 v82, v73, v74 op_sel:[0,0,1]
	v_med3_f32 v61, v62, s95, v189
	v_med3_f32 v62, v63, s95, v189
	v_med3_f32 v57, v58, s95, v189
	v_med3_f32 v58, v59, s95, v189
	v_med3_f32 v53, v54, s95, v189
	v_med3_f32 v54, v55, s95, v189
	v_add_co_u32_e32 v52, vcc, s9, v0
	v_pk_mul_f32 v[46:47], v[46:47], s[74:75] op_sel_hi:[1,0]
	v_pk_mul_f32 v[42:43], v[42:43], s[74:75] op_sel_hi:[1,0]
	v_pk_mul_f32 v[38:39], v[38:39], s[74:75] op_sel_hi:[1,0]
	v_cvt_pk_fp8_f32 v19, v3, v4
	global_store_dwordx4 v[0:1], v[128:131], off
	v_cvt_pk_fp8_f32 v65, v61, v62 op_sel:[0,0,1]
	v_cvt_pk_fp8_f32 v66, v57, v58 op_sel:[0,0,1]
	v_cvt_pk_fp8_f32 v67, v53, v54 op_sel:[0,0,1]
	v_addc_co_u32_e32 v53, vcc, 0, v1, vcc
	v_med3_f32 v45, v46, s95, v189
	v_med3_f32 v46, v47, s95, v189
	v_med3_f32 v41, v42, s95, v189
	v_med3_f32 v42, v43, s95, v189
	v_med3_f32 v37, v38, s95, v189
	v_med3_f32 v38, v39, s95, v189
	s_mov_b32 s9, 0x24000
	v_pk_mul_f32 v[30:31], v[30:31], s[74:75] op_sel_hi:[1,0]
	v_pk_mul_f32 v[26:27], v[26:27], s[74:75] op_sel_hi:[1,0]
	v_pk_mul_f32 v[22:23], v[22:23], s[74:75] op_sel_hi:[1,0]
	global_store_dwordx4 v[100:101], v[112:115], off
	v_cvt_pk_fp8_f32 v49, v45, v46 op_sel:[0,0,1]
	v_cvt_pk_fp8_f32 v50, v41, v42 op_sel:[0,0,1]
	v_cvt_pk_fp8_f32 v51, v37, v38 op_sel:[0,0,1]
	v_add_co_u32_e32 v36, vcc, s9, v0
	v_med3_f32 v29, v30, s95, v189
	v_med3_f32 v30, v31, s95, v189
	v_med3_f32 v25, v26, s95, v189
	v_med3_f32 v26, v27, s95, v189
	v_med3_f32 v21, v22, s95, v189
	v_med3_f32 v22, v23, s95, v189
	v_pk_mul_f32 v[14:15], v[14:15], s[74:75] op_sel_hi:[1,0]
	v_pk_mul_f32 v[10:11], v[10:11], s[74:75] op_sel_hi:[1,0]
	v_pk_mul_f32 v[6:7], v[6:7], s[74:75] op_sel_hi:[1,0]
	global_store_dwordx4 v[84:85], v[96:99], off
	v_addc_co_u32_e32 v37, vcc, 0, v1, vcc
	v_cvt_pk_fp8_f32 v33, v29, v30 op_sel:[0,0,1]
	v_cvt_pk_fp8_f32 v34, v25, v26 op_sel:[0,0,1]
	v_cvt_pk_fp8_f32 v35, v21, v22 op_sel:[0,0,1]
	s_mov_b32 s9, 0x28000
	v_med3_f32 v13, v14, s95, v189
	v_med3_f32 v14, v15, s95, v189
	v_med3_f32 v9, v10, s95, v189
	v_med3_f32 v10, v11, s95, v189
	v_med3_f32 v5, v6, s95, v189
	v_med3_f32 v6, v7, s95, v189
	global_store_dwordx4 v[68:69], v[80:83], off
	v_add_co_u32_e32 v20, vcc, s9, v0
	v_cvt_pk_fp8_f32 v17, v13, v14 op_sel:[0,0,1]
	v_cvt_pk_fp8_f32 v18, v9, v10 op_sel:[0,0,1]
	v_cvt_pk_fp8_f32 v19, v5, v6 op_sel:[0,0,1]
	global_store_dwordx4 v[52:53], v[64:67], off
	v_addc_co_u32_e32 v21, vcc, 0, v1, vcc
	global_store_dwordx4 v[36:37], v[48:51], off
	v_add_co_u32_e32 v0, vcc, 0x2c000, v0
	global_store_dwordx4 v[20:21], v[32:35], off
	s_nop 0
	v_addc_co_u32_e32 v1, vcc, 0, v1, vcc
	global_store_dwordx4 v[0:1], v[16:19], off
	s_mov_b64 s[24:25], -1
	s_and_b64 vcc, exec, s[40:41]
	s_mov_b64 s[40:41], -1
	s_cbranch_vccnz .LBB0_1621
; template <class Epi, class Sched>
; __device__ __forceinline__ void gemm_phase(LAS unsigned char* lds, const int K_, const Sched& S, const Epi& E, const int wave_) {
;     ...
; #pragma unroll
;         for (int a = 0; a < 2; ++a)
; #pragma unroll
;             for (int b = 0; b < 2; ++b)
; #pragma unroll
;                 for (int m = 0; m < 4; ++m)
; #pragma unroll
;                     for (int n = 0; n < 2; ++n) { acc[a][b][m][n] = (f32x4){0.f, 0.f, 0.f, 0.f}; asm volatile("" : "+v"(acc[a][b][m][n])); }
;         cur = nxt; cB = nB; cA = nA; ++ui;
	s_mov_b32 s64, s65
	s_mov_b32 s66, s65
	s_mov_b32 s67, s65
	v_mov_b64_e32 v[4:5], s[64:65]
	v_mov_b64_e32 v[130:131], s[66:67]
	v_mov_b64_e32 v[126:127], s[66:67]
	v_mov_b64_e32 v[114:115], s[66:67]
	v_mov_b64_e32 v[110:111], s[66:67]
	v_mov_b64_e32 v[98:99], s[66:67]
	v_mov_b64_e32 v[94:95], s[66:67]
	v_mov_b64_e32 v[82:83], s[66:67]
	v_mov_b64_e32 v[78:79], s[66:67]
	v_mov_b64_e32 v[122:123], s[66:67]
	v_mov_b64_e32 v[118:119], s[66:67]
	v_mov_b64_e32 v[106:107], s[66:67]
	v_mov_b64_e32 v[102:103], s[66:67]
	v_mov_b64_e32 v[90:91], s[66:67]
	v_mov_b64_e32 v[86:87], s[66:67]
	v_mov_b64_e32 v[74:75], s[66:67]
	v_mov_b64_e32 v[70:71], s[66:67]
	v_mov_b64_e32 v[64:65], s[64:65]
	v_mov_b64_e32 v[60:61], s[64:65]
	v_mov_b64_e32 v[48:49], s[64:65]
	v_mov_b64_e32 v[44:45], s[64:65]
	v_mov_b64_e32 v[32:33], s[64:65]
	v_mov_b64_e32 v[28:29], s[64:65]
	v_mov_b64_e32 v[16:17], s[64:65]
	v_mov_b64_e32 v[12:13], s[64:65]
	v_mov_b64_e32 v[56:57], s[64:65]
	v_mov_b64_e32 v[52:53], s[64:65]
	v_mov_b64_e32 v[40:41], s[64:65]
	v_mov_b64_e32 v[36:37], s[64:65]
	v_mov_b64_e32 v[24:25], s[64:65]
	v_mov_b64_e32 v[20:21], s[64:65]
	v_mov_b64_e32 v[8:9], s[64:65]
	v_mov_b64_e32 v[6:7], s[66:67]
	v_mov_b64_e32 v[128:129], s[64:65]
	v_mov_b64_e32 v[124:125], s[64:65]
	v_mov_b64_e32 v[112:113], s[64:65]
	v_mov_b64_e32 v[108:109], s[64:65]
	v_mov_b64_e32 v[96:97], s[64:65]
	v_mov_b64_e32 v[92:93], s[64:65]
	v_mov_b64_e32 v[80:81], s[64:65]
	v_mov_b64_e32 v[76:77], s[64:65]
	v_mov_b64_e32 v[120:121], s[64:65]
	v_mov_b64_e32 v[116:117], s[64:65]
	v_mov_b64_e32 v[104:105], s[64:65]
	v_mov_b64_e32 v[100:101], s[64:65]
	v_mov_b64_e32 v[88:89], s[64:65]
	v_mov_b64_e32 v[84:85], s[64:65]
	v_mov_b64_e32 v[72:73], s[64:65]
	v_mov_b64_e32 v[68:69], s[64:65]
	v_mov_b64_e32 v[66:67], s[66:67]
	v_mov_b64_e32 v[62:63], s[66:67]
	v_mov_b64_e32 v[50:51], s[66:67]
	v_mov_b64_e32 v[46:47], s[66:67]
	v_mov_b64_e32 v[34:35], s[66:67]
	v_mov_b64_e32 v[30:31], s[66:67]
	v_mov_b64_e32 v[18:19], s[66:67]
	v_mov_b64_e32 v[14:15], s[66:67]
	v_mov_b64_e32 v[58:59], s[66:67]
	v_mov_b64_e32 v[54:55], s[66:67]
	v_mov_b64_e32 v[42:43], s[66:67]
	v_mov_b64_e32 v[38:39], s[66:67]
	v_mov_b64_e32 v[26:27], s[66:67]
	v_mov_b64_e32 v[22:23], s[66:67]
	v_mov_b64_e32 v[10:11], s[66:67]
	s_mov_b64 s[40:41], 0
	s_branch .LBB0_1621
